# ctx rows of P5 (w_out0+residual) and P10 (w_in1 xr half) computed by a hand-written LDS-staged 64x64-tile bf16 MFMA mini-GEMM on all 256 WGs; the main 256x256 GEMMs drop the ctx units (P5 3->2 rounds,
# speedup vs baseline: 1.0160x; 1.0160x over previous
; #define SEAM(k) do { if (IN(k) && IN((k) + 1)) { if ((MK_TAIL_MASK >> (k)) & 1u) moe_pull(F, (k), 0); if ((k) == 9) moe_pull(F, -1, NQ_LATE); if ((k) == 15) moe_pull(F, -1, NQ); xcd_barrier(bar); { int t_ = threadIdx.x; asm volatile("" : "+v"(t_)); F.tid = t_; F.lane = t_ & 63; } } } while (0)
;     __device__ __forceinline__ void operator()(const f32x4 (&acc)[2][2][4][2], const Unit& u, int wr, int wc, int fr, int fq) const {
;     ...
;                         for (int n = 0; n < 2; ++n) bs[m][bj][n] = *(const f32x4*)(res + (size_t)(row0 + ai * HALF + m * 16) * 2048 + col0 + bj * HALF + n * 4);
; #pragma unroll
;                 for (int m = 0; m < 4; ++m)
; #pragma unroll
;                     for (int bj = 0; bj < 2; ++bj) { const f32x4 r0 = bs[m][bj][0] + gg[bj][0] * acc[ai][bj][m][0], r1 = bs[m][bj][1] + gg[bj][1] * acc[ai][bj][m][1];
; __global__ void __launch_bounds__(NWAVES * 64, 2) fwd_kernel(Args args) {
;     ...
;     if (IN(5)) { pg8::Gemm g{WSP(const pg8::bf16_t, WS_AO), WSP(const pg8::bf16_t, WS_WOUT0), MT, DM, DM, 0, DM, 0, 0}; pg8::StaticOrder S; S.init(MT, DM, F.G, (int)blockIdx.x);
;         pg8::EpiResH<false> E{F.in[0], F.in[2], WSP(pg8::bf16_t, WS_H), WSP(const float, WS_MOD0) + 2 * DM, 1.0f};
;         pg8::gemm_phase<pg8::EpiResH<false>, pg8::StaticOrder, true, true>(F.lds, g, S, E); } SEAM(5);
.LBB0_546:
	v_readlane_b32 s98, v250, 62
	v_and_b32_e32 v2, 15, v0
	v_bfe_u32 v3, v0, 4, 2
	v_lshrrev_b32_e32 v4, 6, v0
	v_lshrrev_b32_e32 v5, 1, v4
	v_and_b32_e32 v6, 1, v4
	s_lshr_b32 s99, s98, 5
	s_lshl_b32 s99, s99, 6
	s_and_b32 s100, s98, 31
	s_lshl_b32 s100, s100, 6
	v_lshl_add_u32 v7, v5, 4, v2
	v_add_u32_e32 v7, s99, v7
	v_lshrrev_b32_e32 v8, 4, v0
	v_lshlrev_b32_e32 v9, 4, v2
	v_add_u32_e32 v10, s99, v8
	v_mul_u32_u24_e32 v10, 0x1000, v10
	v_add_u32_e32 v10, v10, v9
	s_mov_b32 s101, 0x25c00000
	v_add_u32_e32 v10, s101, v10
	v_mov_b32_e32 v11, 0
	v_add_u32_e32 v12, 0x20000, v10
	v_mov_b32_e32 v13, 0
	v_add_u32_e32 v14, s100, v8
	v_mul_u32_u24_e32 v14, 0x1000, v14
	v_add_u32_e32 v14, v14, v9
	s_mov_b32 s101, 0x2600000
	v_add_u32_e32 v14, s101, v14
	v_mov_b32_e32 v15, 0
	v_add_u32_e32 v16, 0x20000, v14
	v_mov_b32_e32 v17, 0
	v_lshl_add_u64 v[10:11], s[88:89], 0, v[10:11]
	v_lshl_add_u64 v[12:13], s[88:89], 0, v[12:13]
	v_lshl_add_u64 v[14:15], s[88:89], 0, v[14:15]
	v_lshl_add_u64 v[16:17], s[88:89], 0, v[16:17]
	v_mul_u32_u24_e32 v18, 272, v8
	v_add_u32_e32 v18, v18, v9
	v_lshl_add_u32 v19, v5, 4, v2
	v_mul_u32_u24_e32 v19, 272, v19
	v_lshl_add_u32 v19, v3, 4, v19
	v_lshl_add_u32 v28, v6, 5, v2
	v_mul_u32_u24_e32 v28, 272, v28
	v_lshl_add_u32 v28, v3, 4, v28
	v_add_u32_e32 v28, 17408, v28
	v_mov_b32_e32 v112, 0x200
	v_mov_b32_e32 v113, 0
	v_lshl_add_u32 v116, v6, 5, s100
	v_lshl_add_u32 v116, v3, 2, v116
	v_lshlrev_b32_e32 v118, 2, v116
	v_lshl_add_u32 v128, v7, 13, v118
	v_mov_b32_e32 v129, 0
	v_readlane_b32 s100, v250, 12
	v_readlane_b32 s101, v250, 13
	s_nop 4
	v_lshl_add_u64 v[128:129], s[100:101], 0, v[128:129]
	s_mov_b32 s101, 0x11c000
	v_add_u32_e32 v130, s101, v118
	v_mov_b32_e32 v131, 0
	v_lshl_add_u64 v[130:131], s[88:89], 0, v[130:131]
	global_load_dwordx4 v[132:135], v[128:129], off
	global_load_dwordx4 v[136:139], v[128:129], off offset:64
	global_load_dwordx4 v[140:143], v[130:131], off
	global_load_dwordx4 v[144:147], v[130:131], off offset:64
	v_mov_b32_e32 v20, 0
	v_mov_b32_e32 v21, 0
	v_mov_b32_e32 v22, 0
	v_mov_b32_e32 v23, 0
	v_mov_b32_e32 v24, 0
	v_mov_b32_e32 v25, 0
	v_mov_b32_e32 v26, 0
	v_mov_b32_e32 v27, 0
	global_load_dwordx4 v[32:35], v[10:11], off offset:0
	global_load_dwordx4 v[36:39], v[12:13], off offset:0
	global_load_dwordx4 v[40:43], v[14:15], off offset:0
	global_load_dwordx4 v[44:47], v[16:17], off offset:0
	global_load_dwordx4 v[48:51], v[10:11], off offset:256
	global_load_dwordx4 v[52:55], v[12:13], off offset:256
	global_load_dwordx4 v[56:59], v[14:15], off offset:256
	global_load_dwordx4 v[60:63], v[16:17], off offset:256
	s_waitcnt vmcnt(4)
	ds_write_b128 v18, v[32:35] offset:0
	ds_write_b128 v18, v[36:39] offset:8704
	ds_write_b128 v18, v[40:43] offset:17408
	ds_write_b128 v18, v[44:47] offset:26112
	s_waitcnt lgkmcnt(0)
	s_barrier
	s_mov_b32 s101, 8
; __device__ __forceinline__ unsigned cvt_pk_bf16(float lo, float hi) { unsigned r; asm volatile("v_cvt_pk_bf16_f32 %0, %1, %2" : "=v"(r) : "v"(lo), "v"(hi)); return r; }
;     __device__ __forceinline__ void operator()(const f32x4 (&acc)[2][2][4][2], const Unit& u, int wr, int wc, int fr, int fq) const {
;     ...
;                     for (int bj = 0; bj < 2; ++bj) { const f32x4 r0 = bs[m][bj][0] + gg[bj][0] * acc[ai][bj][m][0], r1 = bs[m][bj][1] + gg[bj][1] * acc[ai][bj][m][1];
;                         u32x4 w; w.x = cvt_pk_bf16(r0[0], r0[1]); w.y = cvt_pk_bf16(r0[2], r0[3]); w.z = cvt_pk_bf16(r1[0], r1[1]); w.w = cvt_pk_bf16(r1[2], r1[3]);
;                         *(u32x4*)(H + (size_t)(row0 + ai * HALF + m * 16) * 2048 + col0 + bj * HALF) = w; }
; __device__ __forceinline__ void xcd_barrier(const XcdBarrier& b) {
;     asm volatile("s_waitcnt vmcnt(0)" ::: "memory");
;     __syncthreads();
;     if (threadIdx.x == 0) {
;         unsigned* bar = b.bar;
;         __builtin_amdgcn_s_waitcnt(0);
;         unsigned nloc = b.st[0], nx = b.st[1];
;         if (nloc == 0u) { xcd_barrier_complete(bar, b.x, b.total, nloc, nx); b.st[0] = nloc; b.st[1] = nx; }
.Lmg5_kloop:
	global_load_dwordx4 v[32:35], v[10:11], off offset:512
	global_load_dwordx4 v[36:39], v[12:13], off offset:512
	global_load_dwordx4 v[40:43], v[14:15], off offset:512
	global_load_dwordx4 v[44:47], v[16:17], off offset:512
	s_waitcnt vmcnt(4)
	ds_write_b128 v18, v[48:51] offset:34816
	ds_write_b128 v18, v[52:55] offset:43520
	ds_write_b128 v18, v[56:59] offset:52224
	ds_write_b128 v18, v[60:63] offset:60928
	ds_read_b128 v[64:67], v19 offset:0
	ds_read_b128 v[68:71], v19 offset:64
	ds_read_b128 v[72:75], v19 offset:128
	ds_read_b128 v[76:79], v19 offset:192
	ds_read_b128 v[80:83], v28 offset:0
	ds_read_b128 v[84:87], v28 offset:64
	ds_read_b128 v[88:91], v28 offset:128
	ds_read_b128 v[92:95], v28 offset:192
	ds_read_b128 v[96:99], v28 offset:4352
	ds_read_b128 v[100:103], v28 offset:4416
	ds_read_b128 v[104:107], v28 offset:4480
	ds_read_b128 v[108:111], v28 offset:4544
	s_waitcnt lgkmcnt(0)
	v_mfma_f32_16x16x32_bf16 v[20:23], v[80:83], v[64:67], v[20:23]
	v_mfma_f32_16x16x32_bf16 v[24:27], v[96:99], v[64:67], v[24:27]
	v_mfma_f32_16x16x32_bf16 v[20:23], v[84:87], v[68:71], v[20:23]
	v_mfma_f32_16x16x32_bf16 v[24:27], v[100:103], v[68:71], v[24:27]
	v_mfma_f32_16x16x32_bf16 v[20:23], v[88:91], v[72:75], v[20:23]
	v_mfma_f32_16x16x32_bf16 v[24:27], v[104:107], v[72:75], v[24:27]
	v_mfma_f32_16x16x32_bf16 v[20:23], v[92:95], v[76:79], v[20:23]
	v_mfma_f32_16x16x32_bf16 v[24:27], v[108:111], v[76:79], v[24:27]
	s_waitcnt lgkmcnt(0)
	s_barrier
	global_load_dwordx4 v[48:51], v[10:11], off offset:768
	global_load_dwordx4 v[52:55], v[12:13], off offset:768
	global_load_dwordx4 v[56:59], v[14:15], off offset:768
	global_load_dwordx4 v[60:63], v[16:17], off offset:768
	s_waitcnt vmcnt(4)
	ds_write_b128 v18, v[32:35] offset:0
	ds_write_b128 v18, v[36:39] offset:8704
	ds_write_b128 v18, v[40:43] offset:17408
	ds_write_b128 v18, v[44:47] offset:26112
	ds_read_b128 v[64:67], v19 offset:34816
	ds_read_b128 v[68:71], v19 offset:34880
	ds_read_b128 v[72:75], v19 offset:34944
	ds_read_b128 v[76:79], v19 offset:35008
	ds_read_b128 v[80:83], v28 offset:34816
	ds_read_b128 v[84:87], v28 offset:34880
	ds_read_b128 v[88:91], v28 offset:34944
	ds_read_b128 v[92:95], v28 offset:35008
	ds_read_b128 v[96:99], v28 offset:39168
	ds_read_b128 v[100:103], v28 offset:39232
	ds_read_b128 v[104:107], v28 offset:39296
	ds_read_b128 v[108:111], v28 offset:39360
	s_waitcnt lgkmcnt(0)
	v_mfma_f32_16x16x32_bf16 v[20:23], v[80:83], v[64:67], v[20:23]
	v_mfma_f32_16x16x32_bf16 v[24:27], v[96:99], v[64:67], v[24:27]
	v_mfma_f32_16x16x32_bf16 v[20:23], v[84:87], v[68:71], v[20:23]
	v_mfma_f32_16x16x32_bf16 v[24:27], v[100:103], v[68:71], v[24:27]
	v_mfma_f32_16x16x32_bf16 v[20:23], v[88:91], v[72:75], v[20:23]
	v_mfma_f32_16x16x32_bf16 v[24:27], v[104:107], v[72:75], v[24:27]
	v_mfma_f32_16x16x32_bf16 v[20:23], v[92:95], v[76:79], v[20:23]
	v_mfma_f32_16x16x32_bf16 v[24:27], v[108:111], v[76:79], v[24:27]
	v_lshl_add_u64 v[10:11], v[10:11], 0, v[112:113]
	v_lshl_add_u64 v[12:13], v[12:13], 0, v[112:113]
	v_lshl_add_u64 v[14:15], v[14:15], 0, v[112:113]
	v_lshl_add_u64 v[16:17], v[16:17], 0, v[112:113]
	s_waitcnt lgkmcnt(0)
	s_barrier
	s_sub_u32 s101, s101, 1
	s_cmp_lg_u32 s101, 0
	s_cbranch_scc1 .Lmg5_kloop
	s_nop 7
	s_nop 7
	v_lshlrev_b32_e32 v116, 1, v116
	v_lshl_add_u32 v116, v7, 12, v116
	s_mov_b32 s101, 0x51800000
	v_add_u32_e32 v116, s101, v116
	v_mov_b32_e32 v117, 0
	v_lshl_add_u64 v[116:117], s[88:89], 0, v[116:117]
	v_fma_f32 v20, v140, v20, v132
	v_fma_f32 v21, v141, v21, v133
	v_fma_f32 v22, v142, v22, v134
	v_fma_f32 v23, v143, v23, v135
	v_fma_f32 v24, v144, v24, v136
	v_fma_f32 v25, v145, v25, v137
	v_fma_f32 v26, v146, v26, v138
	v_fma_f32 v27, v147, v27, v139
	v_cvt_pk_bf16_f32 v28, v20, v21
	v_cvt_pk_bf16_f32 v29, v22, v23
	v_cvt_pk_bf16_f32 v30, v24, v25
	v_cvt_pk_bf16_f32 v31, v26, v27
	global_store_dwordx2 v[116:117], v[28:29], off
	global_store_dwordx2 v[116:117], v[30:31], off offset:32
	s_cmp_gt_i32 s91, 6
	s_cselect_b64 s[0:1], -1, 0
	s_and_b64 s[2:3], s[2:3], s[0:1]
	s_andn2_b64 vcc, exec, s[2:3]
	s_cbranch_vccnz .LBB0_600
	s_waitcnt vmcnt(0)
	s_waitcnt vmcnt(0) lgkmcnt(0)
	s_barrier
	s_mov_b64 s[2:3], exec
	v_readlane_b32 s4, v250, 59
	v_readlane_b32 s5, v250, 60
	s_and_b64 s[4:5], s[2:3], s[4:5]
	s_mov_b64 exec, s[4:5]
	s_cbranch_execz .LBB0_599
	s_add_i32 s4, 0, 0x25020
	v_mov_b32_e32 v1, s4
	s_waitcnt vmcnt(0) expcnt(0) lgkmcnt(0)
	ds_read_b32 v3, v1
	s_add_i32 s4, 0, 0x25024
	v_mov_b32_e32 v1, s4
	ds_read_b32 v1, v1
	s_waitcnt lgkmcnt(1)
	v_cmp_ne_u32_e32 vcc, 0, v3
	s_cbranch_vccnz .LBB0_563
	s_add_u32 s4, s88, 0x4200
	s_addc_u32 s5, s89, 0
	s_add_u32 s6, s88, 0x4400
	s_addc_u32 s7, s89, 0
	s_add_u32 s8, s88, 0x4500
	s_addc_u32 s9, s89, 0
	s_add_u32 s10, s88, 0x4600
	s_addc_u32 s11, s89, 0
	s_add_u32 s12, s88, 0x4700
	s_addc_u32 s13, s89, 0
	s_add_u32 s14, s88, 0x4800
	s_addc_u32 s15, s89, 0
	s_add_u32 s16, s88, 0x4900
	s_addc_u32 s17, s89, 0
	s_add_u32 s18, s88, 0x4a00
	s_addc_u32 s19, s89, 0
	s_add_u32 s20, s88, 0x4b00
	s_addc_u32 s21, s89, 0
	s_add_u32 s22, s88, 0x4c00
	s_addc_u32 s23, s89, 0
	s_add_u32 s24, s88, 0x4d00
	s_addc_u32 s25, s89, 0
	s_add_u32 s26, s88, 0x4e00
	s_addc_u32 s27, s89, 0
	s_add_u32 s28, s88, 0x4f00
	s_addc_u32 s29, s89, 0
	s_add_u32 s30, s88, 0x5000
	s_addc_u32 s31, s89, 0
	s_add_u32 s34, s88, 0x5100
	s_addc_u32 s35, s89, 0
	s_add_u32 s36, s88, 0x5200
	s_addc_u32 s37, s89, 0
	s_add_u32 s38, s88, 0x5300
	s_addc_u32 s39, s89, 0
	s_mov_b32 s33, 1
	v_mov_b32_e32 v17, 0
	s_branch .LBB0_551

; #define SEAM(k) do { if (IN(k) && IN((k) + 1)) { if ((MK_TAIL_MASK >> (k)) & 1u) moe_pull(F, (k), 0); if ((k) == 9) moe_pull(F, -1, NQ_LATE); if ((k) == 15) moe_pull(F, -1, NQ); xcd_barrier(bar); { int t_ = threadIdx.x; asm volatile("" : "+v"(t_)); F.tid = t_; F.lane = t_ & 63; } } } while (0)
; __global__ void __launch_bounds__(NWAVES * 64, 2) fwd_kernel(Args args) {
;     ...
;     if (IN(10)) { pg8::Gemm g{XN, WSP(const pg8::bf16_t, WS_WIN1), MT, 2 * DM, DM, 0, DM, 0, 0}; pg8::StaticOrder S; S.init(MT, 2 * DM, F.G, (int)blockIdx.x);
;         pg8::EpiBf16 E{WSP(pg8::bf16_t, WS_Z), 2 * DM, 8, 0, 1.0f};
;         pg8::gemm_phase<pg8::EpiBf16, pg8::StaticOrder, true, true>(F.lds, g, S, E); } SEAM(10);
.LBB0_1297:
	v_readlane_b32 s98, v250, 62
	v_and_b32_e32 v2, 15, v0
	v_bfe_u32 v3, v0, 4, 2
	v_lshrrev_b32_e32 v4, 6, v0
	v_lshrrev_b32_e32 v5, 1, v4
	v_and_b32_e32 v6, 1, v4
	s_lshr_b32 s99, s98, 5
	s_lshl_b32 s99, s99, 6
	s_and_b32 s100, s98, 31
	s_lshl_b32 s100, s100, 6
	v_lshl_add_u32 v7, v5, 4, v2
	v_add_u32_e32 v7, s99, v7
	v_lshrrev_b32_e32 v8, 4, v0
	v_lshlrev_b32_e32 v9, 4, v2
	v_add_u32_e32 v10, s99, v8
	v_mul_u32_u24_e32 v10, 0x1000, v10
	v_add_u32_e32 v10, v10, v9
	s_mov_b32 s101, 0x21a00000
	v_add_u32_e32 v10, s101, v10
	v_mov_b32_e32 v11, 0
	v_add_u32_e32 v12, 0x20000, v10
	v_mov_b32_e32 v13, 0
	v_add_u32_e32 v14, s100, v8
	v_mul_u32_u24_e32 v14, 0x1000, v14
	v_add_u32_e32 v14, v14, v9
	s_mov_b32 s101, 0x7800000
	v_add_u32_e32 v14, s101, v14
	v_mov_b32_e32 v15, 0
	v_add_u32_e32 v16, 0x20000, v14
	v_mov_b32_e32 v17, 0
	v_lshl_add_u64 v[10:11], s[88:89], 0, v[10:11]
	v_lshl_add_u64 v[12:13], s[88:89], 0, v[12:13]
	v_lshl_add_u64 v[14:15], s[88:89], 0, v[14:15]
	v_lshl_add_u64 v[16:17], s[88:89], 0, v[16:17]
	v_mul_u32_u24_e32 v18, 272, v8
	v_add_u32_e32 v18, v18, v9
	v_lshl_add_u32 v19, v5, 4, v2
	v_mul_u32_u24_e32 v19, 272, v19
	v_lshl_add_u32 v19, v3, 4, v19
	v_lshl_add_u32 v28, v6, 5, v2
	v_mul_u32_u24_e32 v28, 272, v28
	v_lshl_add_u32 v28, v3, 4, v28
	v_add_u32_e32 v28, 17408, v28
	v_mov_b32_e32 v112, 0x200
	v_mov_b32_e32 v113, 0
	v_mov_b32_e32 v20, 0
	v_mov_b32_e32 v21, 0
	v_mov_b32_e32 v22, 0
	v_mov_b32_e32 v23, 0
	v_mov_b32_e32 v24, 0
	v_mov_b32_e32 v25, 0
	v_mov_b32_e32 v26, 0
	v_mov_b32_e32 v27, 0
	global_load_dwordx4 v[32:35], v[10:11], off offset:0
	global_load_dwordx4 v[36:39], v[12:13], off offset:0
	global_load_dwordx4 v[40:43], v[14:15], off offset:0
	global_load_dwordx4 v[44:47], v[16:17], off offset:0
	global_load_dwordx4 v[48:51], v[10:11], off offset:256
	global_load_dwordx4 v[52:55], v[12:13], off offset:256
	global_load_dwordx4 v[56:59], v[14:15], off offset:256
	global_load_dwordx4 v[60:63], v[16:17], off offset:256
	s_waitcnt vmcnt(4)
	ds_write_b128 v18, v[32:35] offset:0
	ds_write_b128 v18, v[36:39] offset:8704
	ds_write_b128 v18, v[40:43] offset:17408
	ds_write_b128 v18, v[44:47] offset:26112
	s_waitcnt lgkmcnt(0)
	s_barrier
	s_mov_b32 s101, 8
; __device__ __forceinline__ unsigned cvt_pk_bf16(float lo, float hi) { unsigned r; asm volatile("v_cvt_pk_bf16_f32 %0, %1, %2" : "=v"(r) : "v"(lo), "v"(hi)); return r; }
;     __device__ __forceinline__ void operator()(const f32x4 (&acc)[2][2][4][2], const Unit& u, int wr, int wc, int fr, int fq) const {
;     ...
;                     u32x4 w; w.x = cvt_pk_bf16(v0[0], v0[1]); w.y = cvt_pk_bf16(v0[2], v0[3]); w.z = cvt_pk_bf16(v1[0], v1[1]); w.w = cvt_pk_bf16(v1[2], v1[3]);
;                     *(u32x4*)(rowp + bj * HALF) = w; } }
; __device__ __forceinline__ void xcd_barrier(const XcdBarrier& b) {
;     asm volatile("s_waitcnt vmcnt(0)" ::: "memory");
;     __syncthreads();
;     if (threadIdx.x == 0) {
;         unsigned* bar = b.bar;
;         __builtin_amdgcn_s_waitcnt(0);
;         unsigned nloc = b.st[0], nx = b.st[1];
;         if (nloc == 0u) { xcd_barrier_complete(bar, b.x, b.total, nloc, nx); b.st[0] = nloc; b.st[1] = nx; }
.Lmg10_kloop:
	global_load_dwordx4 v[32:35], v[10:11], off offset:512
	global_load_dwordx4 v[36:39], v[12:13], off offset:512
	global_load_dwordx4 v[40:43], v[14:15], off offset:512
	global_load_dwordx4 v[44:47], v[16:17], off offset:512
	s_waitcnt vmcnt(4)
	ds_write_b128 v18, v[48:51] offset:34816
	ds_write_b128 v18, v[52:55] offset:43520
	ds_write_b128 v18, v[56:59] offset:52224
	ds_write_b128 v18, v[60:63] offset:60928
	ds_read_b128 v[64:67], v19 offset:0
	ds_read_b128 v[68:71], v19 offset:64
	ds_read_b128 v[72:75], v19 offset:128
	ds_read_b128 v[76:79], v19 offset:192
	ds_read_b128 v[80:83], v28 offset:0
	ds_read_b128 v[84:87], v28 offset:64
	ds_read_b128 v[88:91], v28 offset:128
	ds_read_b128 v[92:95], v28 offset:192
	ds_read_b128 v[96:99], v28 offset:4352
	ds_read_b128 v[100:103], v28 offset:4416
	ds_read_b128 v[104:107], v28 offset:4480
	ds_read_b128 v[108:111], v28 offset:4544
	s_waitcnt lgkmcnt(0)
	v_mfma_f32_16x16x32_bf16 v[20:23], v[80:83], v[64:67], v[20:23]
	v_mfma_f32_16x16x32_bf16 v[24:27], v[96:99], v[64:67], v[24:27]
	v_mfma_f32_16x16x32_bf16 v[20:23], v[84:87], v[68:71], v[20:23]
	v_mfma_f32_16x16x32_bf16 v[24:27], v[100:103], v[68:71], v[24:27]
	v_mfma_f32_16x16x32_bf16 v[20:23], v[88:91], v[72:75], v[20:23]
	v_mfma_f32_16x16x32_bf16 v[24:27], v[104:107], v[72:75], v[24:27]
	v_mfma_f32_16x16x32_bf16 v[20:23], v[92:95], v[76:79], v[20:23]
	v_mfma_f32_16x16x32_bf16 v[24:27], v[108:111], v[76:79], v[24:27]
	s_waitcnt lgkmcnt(0)
	s_barrier
	global_load_dwordx4 v[48:51], v[10:11], off offset:768
	global_load_dwordx4 v[52:55], v[12:13], off offset:768
	global_load_dwordx4 v[56:59], v[14:15], off offset:768
	global_load_dwordx4 v[60:63], v[16:17], off offset:768
	s_waitcnt vmcnt(4)
	ds_write_b128 v18, v[32:35] offset:0
	ds_write_b128 v18, v[36:39] offset:8704
	ds_write_b128 v18, v[40:43] offset:17408
	ds_write_b128 v18, v[44:47] offset:26112
	ds_read_b128 v[64:67], v19 offset:34816
	ds_read_b128 v[68:71], v19 offset:34880
	ds_read_b128 v[72:75], v19 offset:34944
	ds_read_b128 v[76:79], v19 offset:35008
	ds_read_b128 v[80:83], v28 offset:34816
	ds_read_b128 v[84:87], v28 offset:34880
	ds_read_b128 v[88:91], v28 offset:34944
	ds_read_b128 v[92:95], v28 offset:35008
	ds_read_b128 v[96:99], v28 offset:39168
	ds_read_b128 v[100:103], v28 offset:39232
	ds_read_b128 v[104:107], v28 offset:39296
	ds_read_b128 v[108:111], v28 offset:39360
	s_waitcnt lgkmcnt(0)
	v_mfma_f32_16x16x32_bf16 v[20:23], v[80:83], v[64:67], v[20:23]
	v_mfma_f32_16x16x32_bf16 v[24:27], v[96:99], v[64:67], v[24:27]
	v_mfma_f32_16x16x32_bf16 v[20:23], v[84:87], v[68:71], v[20:23]
	v_mfma_f32_16x16x32_bf16 v[24:27], v[100:103], v[68:71], v[24:27]
	v_mfma_f32_16x16x32_bf16 v[20:23], v[88:91], v[72:75], v[20:23]
	v_mfma_f32_16x16x32_bf16 v[24:27], v[104:107], v[72:75], v[24:27]
	v_mfma_f32_16x16x32_bf16 v[20:23], v[92:95], v[76:79], v[20:23]
	v_mfma_f32_16x16x32_bf16 v[24:27], v[108:111], v[76:79], v[24:27]
	v_lshl_add_u64 v[10:11], v[10:11], 0, v[112:113]
	v_lshl_add_u64 v[12:13], v[12:13], 0, v[112:113]
	v_lshl_add_u64 v[14:15], v[14:15], 0, v[112:113]
	v_lshl_add_u64 v[16:17], v[16:17], 0, v[112:113]
	s_waitcnt lgkmcnt(0)
	s_barrier
	s_sub_u32 s101, s101, 1
	s_cmp_lg_u32 s101, 0
	s_cbranch_scc1 .Lmg10_kloop
	s_nop 7
	s_nop 7
	v_lshl_add_u32 v116, v6, 5, s100
	v_lshl_add_u32 v116, v3, 2, v116
	v_lshlrev_b32_e32 v116, 1, v116
	v_lshl_add_u32 v116, v7, 13, v116
	s_mov_b32 s101, 0x2e701000
	v_add_u32_e32 v116, s101, v116
	v_mov_b32_e32 v117, 0
	v_lshl_add_u64 v[116:117], s[88:89], 0, v[116:117]
	v_cvt_pk_bf16_f32 v28, v20, v21
	v_cvt_pk_bf16_f32 v29, v22, v23
	v_cvt_pk_bf16_f32 v30, v24, v25
	v_cvt_pk_bf16_f32 v31, v26, v27
	global_store_dwordx2 v[116:117], v[28:29], off
	global_store_dwordx2 v[116:117], v[30:31], off offset:32
	s_cmp_gt_i32 s91, 11
	s_cselect_b64 s[0:1], -1, 0
	s_and_b64 s[2:3], s[4:5], s[0:1]
	s_andn2_b64 vcc, exec, s[2:3]
	s_cbranch_vccnz .LBB0_1351
	s_waitcnt vmcnt(0)
	s_waitcnt vmcnt(0) lgkmcnt(0)
	s_barrier
	s_mov_b64 s[2:3], exec
	v_readlane_b32 s4, v250, 59
	v_readlane_b32 s5, v250, 60
	s_and_b64 s[4:5], s[2:3], s[4:5]
	s_mov_b64 exec, s[4:5]
	s_cbranch_execz .LBB0_1350
	s_add_i32 s4, 0, 0x25020
	v_mov_b32_e32 v1, s4
	s_waitcnt vmcnt(0) expcnt(0) lgkmcnt(0)
	ds_read_b32 v3, v1
	s_add_i32 s4, 0, 0x25024
	v_mov_b32_e32 v1, s4
	ds_read_b32 v1, v1
	s_waitcnt lgkmcnt(1)
	v_cmp_ne_u32_e32 vcc, 0, v3
	s_cbranch_vccnz .LBB0_1314
	s_add_u32 s4, s88, 0x4200
	s_addc_u32 s5, s89, 0
	s_add_u32 s6, s88, 0x4400
	s_addc_u32 s7, s89, 0
	s_add_u32 s8, s88, 0x4500
	s_addc_u32 s9, s89, 0
	s_add_u32 s10, s88, 0x4600
	s_addc_u32 s11, s89, 0
	s_add_u32 s12, s88, 0x4700
	s_addc_u32 s13, s89, 0
	s_add_u32 s14, s88, 0x4800
	s_addc_u32 s15, s89, 0
	s_add_u32 s16, s88, 0x4900
	s_addc_u32 s17, s89, 0
	s_add_u32 s18, s88, 0x4a00
	s_addc_u32 s19, s89, 0
	s_add_u32 s20, s88, 0x4b00
	s_addc_u32 s21, s89, 0
	s_add_u32 s22, s88, 0x4c00
	s_addc_u32 s23, s89, 0
	s_add_u32 s24, s88, 0x4d00
	s_addc_u32 s25, s89, 0
	s_add_u32 s26, s88, 0x4e00
	s_addc_u32 s27, s89, 0
	s_add_u32 s28, s88, 0x4f00
	s_addc_u32 s29, s89, 0
	s_add_u32 s30, s88, 0x5000
	s_addc_u32 s31, s89, 0
	s_add_u32 s34, s88, 0x5100
	s_addc_u32 s35, s89, 0
	s_add_u32 s36, s88, 0x5200
	s_addc_u32 s37, s89, 0
	s_add_u32 s38, s88, 0x5300
	s_addc_u32 s39, s89, 0
	s_mov_b32 s33, 1
	v_mov_b32_e32 v17, 0
	s_branch .LBB0_1302
